# norm phase prologues: the two gain-vector loads issued with the nine modulation-vector loads instead of two trailing load-wait-write round trips
# speedup vs baseline: 1.0068x; 1.0068x over previous
.LBB0_1514:
	s_or_b64 exec, exec, s[4:5]
	v_lshlrev_b32_e32 v20, 2, v23
	v_ashrrev_i32_e32 v21, 31, v20
	v_lshlrev_b64 v[20:21], 2, v[20:21]
	v_lshl_add_u64 v[64:65], s[40:41], 0, v[20:21]
	v_add_co_u32_e32 v52, vcc, 0xc000, v64
	v_lshl_add_u64 v[68:69], s[44:45], 0, v[20:21]
	s_nop 0
	v_addc_co_u32_e32 v53, vcc, 0, v65, vcc
	v_add_co_u32_e32 v56, vcc, 0xc000, v68
	v_lshl_add_u64 v[72:73], s[46:47], 0, v[20:21]
	s_nop 0
	v_addc_co_u32_e32 v57, vcc, 0, v69, vcc
	global_load_dwordx4 v[24:27], v[64:65], off
	global_load_dwordx4 v[44:47], v[68:69], off
	global_load_dwordx4 v[48:51], v[72:73], off
	v_add_co_u32_e32 v60, vcc, 0xc000, v72
	global_load_dwordx4 v[52:55], v[52:53], off
	s_nop 0
	v_addc_co_u32_e32 v61, vcc, 0, v73, vcc
	v_add_co_u32_e32 v64, vcc, 0x18000, v64
	global_load_dwordx4 v[56:59], v[56:57], off
	s_nop 0
	v_addc_co_u32_e32 v65, vcc, 0, v65, vcc
	v_add_co_u32_e32 v68, vcc, 0x18000, v68
	global_load_dwordx4 v[60:63], v[60:61], off
	s_nop 0
	v_addc_co_u32_e32 v69, vcc, 0, v69, vcc
	global_load_dwordx4 v[64:67], v[64:65], off
	v_add_co_u32_e32 v72, vcc, 0x18000, v72
	global_load_dwordx4 v[68:71], v[68:69], off
	s_nop 0
	v_addc_co_u32_e32 v73, vcc, 0, v73, vcc
	global_load_dwordx4 v[72:75], v[72:73], off
	v_lshl_add_u32 v2, v23, 4, 0
	v_add_u32_e32 v23, 0xc000, v2
	v_lshl_add_u64 v[182:183], s[36:37], 0, v[20:21]
	global_load_dwordx4 v[182:185], v[182:183], off
	v_lshl_add_u64 v[178:179], s[38:39], 0, v[20:21]
	global_load_dwordx4 v[178:181], v[178:179], off
	s_waitcnt vmcnt(10)
	ds_write_b128 v2, v[24:27]
	s_waitcnt vmcnt(9)
	ds_write_b128 v2, v[44:47] offset:24576
	s_waitcnt vmcnt(8)
	ds_write_b128 v2, v[48:51] offset:49152
	s_waitcnt vmcnt(7)
	ds_write_b128 v2, v[52:55] offset:8192
	s_waitcnt vmcnt(6)
	ds_write_b128 v2, v[56:59] offset:32768
	s_waitcnt vmcnt(5)
	ds_write_b128 v2, v[60:63] offset:57344
	s_waitcnt vmcnt(4)
	ds_write_b128 v2, v[64:67] offset:16384
	s_waitcnt vmcnt(3)
	ds_write_b128 v2, v[68:71] offset:40960
	s_waitcnt vmcnt(2)
	ds_write_b128 v23, v[72:75] offset:16384
	v_add_u32_e32 v23, 0x12000, v2
	v_add_u32_e32 v2, 0x14000, v2
	s_waitcnt vmcnt(1)
	ds_write_b128 v23, v[182:185]
	s_waitcnt vmcnt(0)
	ds_write_b128 v2, v[178:181]
	s_waitcnt lgkmcnt(0)
	s_barrier
	s_and_saveexec_b64 s[4:5], s[0:1]
	s_cbranch_execz .LBB0_1530
	s_mul_i32 s0, s14, s93
	v_readlane_b32 s1, v249, 33
	s_sub_i32 s52, s0, s1
	v_lshlrev_b32_e32 v20, 4, v22
	s_add_i32 s0, 0, 0x12000
	v_add_u32_e32 v97, s0, v20
	s_add_i32 s0, 0, 0x14000
	v_add_u32_e32 v98, s0, v20
	v_readlane_b32 s0, v253, 22
	v_lshlrev_b32_e32 v2, 2, v22
	v_lshlrev_b32_e32 v22, 3, v22
	v_mov_b32_e32 v23, v3
	v_readlane_b32 s1, v253, 23
	v_add_u32_e32 v96, 0, v20
	s_addk_i32 s52, 0x2000
	v_lshl_add_u64 v[20:21], s[0:1], 0, v[22:23]
	v_readlane_b32 s0, v249, 52
	v_readlane_b32 s1, v249, 53
	s_mov_b64 s[14:15], 0
	s_nop 0
	v_lshl_add_u64 v[22:23], s[0:1], 0, v[22:23]
	v_readlane_b32 s0, v254, 38
	v_readlane_b32 s1, v254, 39
	s_nop 1
	v_lshl_add_u64 v[24:25], s[0:1], 0, v[2:3]
	v_lshlrev_b32_e32 v2, 1, v2
	s_branch .LBB0_1517

.LBB0_1540:
	s_or_b64 exec, exec, s[14:15]
	v_lshlrev_b32_e32 v36, 2, v39
	v_ashrrev_i32_e32 v37, 31, v36
	v_lshlrev_b64 v[36:37], 2, v[36:37]
	v_lshl_add_u64 v[64:65], s[40:41], 0, v[36:37]
	v_add_co_u32_e32 v52, vcc, 0xc000, v64
	v_lshl_add_u64 v[84:85], s[44:45], 0, v[36:37]
	s_nop 0
	v_addc_co_u32_e32 v53, vcc, 0, v65, vcc
	v_add_co_u32_e32 v56, vcc, 0xc000, v84
	v_lshl_add_u64 v[88:89], s[46:47], 0, v[36:37]
	s_nop 0
	v_addc_co_u32_e32 v57, vcc, 0, v85, vcc
	global_load_dwordx4 v[40:43], v[64:65], off
	global_load_dwordx4 v[44:47], v[84:85], off
	global_load_dwordx4 v[48:51], v[88:89], off
	v_add_co_u32_e32 v60, vcc, 0xc000, v88
	global_load_dwordx4 v[52:55], v[52:53], off
	s_nop 0
	v_addc_co_u32_e32 v61, vcc, 0, v89, vcc
	v_add_co_u32_e32 v64, vcc, 0x18000, v64
	global_load_dwordx4 v[56:59], v[56:57], off
	s_nop 0
	v_addc_co_u32_e32 v65, vcc, 0, v65, vcc
	v_add_co_u32_e32 v84, vcc, 0x18000, v84
	global_load_dwordx4 v[60:63], v[60:61], off
	s_nop 0
	v_addc_co_u32_e32 v85, vcc, 0, v85, vcc
	global_load_dwordx4 v[64:67], v[64:65], off
	v_add_co_u32_e32 v88, vcc, 0x18000, v88
	global_load_dwordx4 v[84:87], v[84:85], off
	s_nop 0
	v_addc_co_u32_e32 v89, vcc, 0, v89, vcc
	global_load_dwordx4 v[88:91], v[88:89], off
	v_lshl_add_u32 v2, v39, 4, 0
	v_add_u32_e32 v39, 0xc000, v2
	v_lshl_add_u64 v[182:183], s[36:37], 0, v[36:37]
	global_load_dwordx4 v[182:185], v[182:183], off
	v_lshl_add_u64 v[178:179], s[38:39], 0, v[36:37]
	global_load_dwordx4 v[178:181], v[178:179], off
	s_waitcnt vmcnt(10)
	ds_write_b128 v2, v[40:43]
	s_waitcnt vmcnt(9)
	ds_write_b128 v2, v[44:47] offset:24576
	s_waitcnt vmcnt(8)
	ds_write_b128 v2, v[48:51] offset:49152
	s_waitcnt vmcnt(7)
	ds_write_b128 v2, v[52:55] offset:8192
	s_waitcnt vmcnt(6)
	ds_write_b128 v2, v[56:59] offset:32768
	s_waitcnt vmcnt(5)
	ds_write_b128 v2, v[60:63] offset:57344
	s_waitcnt vmcnt(4)
	ds_write_b128 v2, v[64:67] offset:16384
	s_waitcnt vmcnt(3)
	ds_write_b128 v2, v[84:87] offset:40960
	s_waitcnt vmcnt(2)
	ds_write_b128 v39, v[88:91] offset:16384
	v_add_u32_e32 v39, 0x12000, v2
	v_add_u32_e32 v2, 0x14000, v2
	s_waitcnt vmcnt(1)
	ds_write_b128 v39, v[182:185]
	s_waitcnt vmcnt(0)
	ds_write_b128 v2, v[178:181]
	s_waitcnt lgkmcnt(0)
	s_barrier
	s_and_saveexec_b64 s[14:15], s[0:1]
	s_cbranch_execz .LBB0_1556
	v_lshlrev_b32_e32 v2, 4, v38
	s_add_i32 s0, 0, 0x12000
	v_add_u32_e32 v131, s0, v2
	s_add_i32 s0, 0, 0x14000
	v_add_u32_e32 v132, s0, v2
	v_readlane_b32 s0, v253, 22
	v_add_u32_e32 v130, 0, v2
	v_lshlrev_b32_e32 v2, 3, v38
	v_readlane_b32 s1, v253, 23
	v_lshlrev_b32_e32 v84, 2, v38
	v_mov_b32_e32 v85, v3
	v_lshl_add_u64 v[86:87], s[0:1], 0, v[2:3]
	v_readlane_b32 s0, v249, 52
	v_readlane_b32 s1, v249, 53
	s_mov_b64 s[48:49], 0
	s_nop 0
	v_lshl_add_u64 v[88:89], s[0:1], 0, v[2:3]
	v_readlane_b32 s0, v254, 38
	v_readlane_b32 s1, v254, 39
	v_lshlrev_b32_e32 v2, 1, v84
	s_nop 0
	v_lshl_add_u64 v[90:91], s[0:1], 0, v[84:85]
	s_branch .LBB0_1543

.LBB0_2021:
	s_or_b64 exec, exec, s[4:5]
	v_readlane_b32 s0, v255, 36
	v_readlane_b32 s1, v255, 37
	v_lshlrev_b32_e32 v12, 2, v15
	s_and_b64 s[0:1], s[0:1], exec
	v_ashrrev_i32_e32 v13, 31, v12
	s_cselect_b32 s5, s45, 0
	s_cselect_b32 s4, s44, 0
	v_lshlrev_b64 v[12:13], 2, v[12:13]
	s_cselect_b32 s1, s41, 0
	s_cselect_b32 s0, s40, 0
	v_lshl_add_u64 v[64:65], s[38:39], 0, v[12:13]
	v_lshl_add_u64 v[72:73], s[4:5], 0, v[12:13]
	s_mov_b32 s4, 0xc000
	v_lshl_add_u64 v[68:69], s[0:1], 0, v[12:13]
	v_add_co_u32_e64 v52, s[0:1], s4, v64
	global_load_dwordx4 v[20:23], v[64:65], off
	global_load_dwordx4 v[24:27], v[68:69], off
	global_load_dwordx4 v[32:35], v[72:73], off
	v_addc_co_u32_e64 v53, s[0:1], 0, v65, s[0:1]
	v_add_co_u32_e64 v56, s[0:1], s4, v68
	global_load_dwordx4 v[52:55], v[52:53], off
	s_nop 0
	v_addc_co_u32_e64 v57, s[0:1], 0, v69, s[0:1]
	v_add_co_u32_e64 v60, s[0:1], s4, v72
	s_mov_b32 s4, 0x18000
	s_nop 0
	v_addc_co_u32_e64 v61, s[0:1], 0, v73, s[0:1]
	v_add_co_u32_e64 v64, s[0:1], s4, v64
	global_load_dwordx4 v[56:59], v[56:57], off
	s_nop 0
	v_addc_co_u32_e64 v65, s[0:1], 0, v65, s[0:1]
	v_add_co_u32_e64 v68, s[0:1], s4, v68
	global_load_dwordx4 v[60:63], v[60:61], off
	s_nop 0
	v_addc_co_u32_e64 v69, s[0:1], 0, v69, s[0:1]
	global_load_dwordx4 v[64:67], v[64:65], off
	v_add_co_u32_e64 v72, s[0:1], s4, v72
	global_load_dwordx4 v[68:71], v[68:69], off
	s_nop 0
	v_addc_co_u32_e64 v73, s[0:1], 0, v73, s[0:1]
	global_load_dwordx4 v[72:75], v[72:73], off
	v_lshl_add_u32 v2, v15, 4, 0
	v_add_u32_e32 v15, 0xc000, v2
	v_lshl_add_u64 v[182:183], s[14:15], 0, v[12:13]
	global_load_dwordx4 v[182:185], v[182:183], off
	v_lshl_add_u64 v[178:179], s[36:37], 0, v[12:13]
	global_load_dwordx4 v[178:181], v[178:179], off
	s_waitcnt vmcnt(10)
	ds_write_b128 v2, v[20:23]
	s_waitcnt vmcnt(9)
	ds_write_b128 v2, v[24:27] offset:24576
	s_waitcnt vmcnt(8)
	ds_write_b128 v2, v[32:35] offset:49152
	s_waitcnt vmcnt(7)
	ds_write_b128 v2, v[52:55] offset:8192
	s_waitcnt vmcnt(6)
	ds_write_b128 v2, v[56:59] offset:32768
	s_waitcnt vmcnt(5)
	ds_write_b128 v2, v[60:63] offset:57344
	s_waitcnt vmcnt(4)
	ds_write_b128 v2, v[64:67] offset:16384
	s_waitcnt vmcnt(3)
	ds_write_b128 v2, v[68:71] offset:40960
	s_waitcnt vmcnt(2)
	ds_write_b128 v15, v[72:75] offset:16384
	v_add_u32_e32 v15, 0x12000, v2
	v_add_u32_e32 v2, 0x14000, v2
	s_waitcnt vmcnt(1)
	ds_write_b128 v15, v[182:185]
	s_waitcnt vmcnt(0)
	ds_write_b128 v2, v[178:181]
	s_waitcnt lgkmcnt(0)
	s_barrier
	s_and_saveexec_b64 s[46:47], vcc
	s_cbranch_execz .LBB0_2077
	v_readlane_b32 s0, v255, 36
	v_readlane_b32 s1, v255, 37
	s_and_b64 s[0:1], s[0:1], exec
	v_readlane_b32 s0, v254, 38
	v_readlane_b32 s1, v254, 39
	s_mul_i32 s4, s12, s93
	v_readlane_b32 s5, v249, 33
	s_cselect_b32 s1, s1, 0
	s_cselect_b32 s0, s0, 0
	s_sub_i32 s51, s4, s5
	v_lshlrev_b32_e32 v12, 4, v14
	s_add_i32 s4, 0, 0x12000
	v_add_u32_e32 v127, s4, v12
	s_add_i32 s4, 0, 0x14000
	v_add_u32_e32 v128, s4, v12
	v_readlane_b32 s4, v253, 22
	v_lshlrev_b32_e32 v52, 3, v14
	v_mov_b32_e32 v53, v3
	v_readlane_b32 s5, v253, 23
	v_lshl_add_u64 v[58:59], s[0:1], 0, v[52:53]
	v_readlane_b32 s0, v254, 61
	v_lshl_add_u64 v[54:55], s[4:5], 0, v[52:53]
	v_readlane_b32 s4, v249, 52
	v_lshlrev_b32_e32 v2, 2, v14
	v_readlane_b32 s5, v249, 53
	v_readlane_b32 s1, v254, 62
	s_addk_i32 s51, 0x2000
	v_add_u32_e32 v126, 0, v12
	v_lshl_add_u64 v[56:57], s[4:5], 0, v[52:53]
	v_lshl_add_u64 v[60:61], s[0:1], 0, v[52:53]
	v_add_u32_e32 v129, 0xffffe000, v1
	s_mov_b64 s[48:49], 0
	v_lshlrev_b32_e32 v2, 1, v2
	s_branch .LBB0_2024
